# v12 + LRU scan unit prologue: 11 serialized parameter loads issued together, one wait
# speedup vs baseline: 1.0041x; 1.0041x over previous
; __device__ __forceinline__ float fast_exp(float x) { return __builtin_amdgcn_exp2f(x * LOG2E); }
; #define LRU_LOAD_RAW(st_) do { const int t_ = ck * TC + (st_) * 32 + r32; const size_t m_ = (size_t)b * SEQ + t_; _Pragma("unroll") for (int ks = 0; ks < 4; ++ks) _Pragma("unroll") for (int j = 0; j < 4; ++j) { \
;             const int back_ = 3 - j; const size_t mm_ = (t_ >= back_) ? m_ - back_ : m_; raw[ks][j] = *(const u32x4*)(U + mm_ * NIN + C_LX + ch0 + 16 * ks + 8 * hi); } } while (0)
; __device__ __forceinline__ void lru_scan(LAS unsigned char* lds, const bf16* U, bf16* HR, bf16* PQ, float* AGG, const bf16* Wt, const float* conv_w, const float* conv_b,
;                                          const float* b_rg, const float* b_ig, const float* lam, int G, int c, int wbase) {
;     ...
;         for (int j = 0; j < 4; ++j) cw[j * 64 + lane] = conv_w[j * DM + ch0 + lane];
;         cw[4 * 64 + lane] = conv_b[ch0 + lane];
;         float brg[2], big[2], sp8[2], carry[2], prodA[2];
; #pragma unroll
;         for (int ct = 0; ct < 2; ++ct) { const int ch = ch0 + 32 * ct + r32; brg[ct] = b_rg[ch] * -LOG2E; big[ct] = b_ig[ch] * -LOG2E; { const float x = fast_exp(-lam[ch]); sp8[ct] = (-8.f * LOG2E) * (x < 0.25f ? x * (1.f - x * (0.5f - x * ((1.f / 3.f) - x * (0.25f - x * (0.2f - x * (1.f / 6.f)))))) : (__builtin_amdgcn_logf(1.f + x) * 0.6931471805599453f)); } carry[ct] = 0.f; prodA[ct] = 1.f; }
;         asm volatile("s_waitcnt lgkmcnt(0)" ::: "memory");
;         u32x4 raw[4][4];
;     ...
;         LRU_LOAD_RAW(0);
.LBB0_595:
	v_or_b32_e32 v0, s30, v145
	v_lshlrev_b32_e32 v232, 2, v0
	v_or_b32_e32 v0, s30, v144
	v_add_u32_e32 v12, 0x1000, v232
	v_add_u32_e32 v13, 0x2000, v232
	global_load_dword v4, v232, s[18:19]
	global_load_dword v8, v12, s[18:19]
	v_add_u32_e32 v12, 0x3000, v232
	global_load_dword v9, v13, s[18:19]
	global_load_dword v10, v12, s[18:19]
	global_load_dword v11, v232, s[20:21]
	v_lshlrev_b32_e32 v232, 2, v0
	global_load_dword v0, v232, s[22:23]
	global_load_dword v1, v232, s[24:25]
	global_load_dword v2, v232, s[26:27]
	global_load_dword v15, v232, s[26:27] offset:128
	global_load_dword v14, v232, s[22:23] offset:128
	global_load_dword v5, v232, s[24:25] offset:128
	s_waitcnt vmcnt(0)
	ds_write2st64_b32 v151, v4, v8 offset0:32 offset1:33
	ds_write2st64_b32 v151, v9, v10 offset0:34 offset1:35
	ds_write_b32 v151, v11 offset:9216
	v_mov_b32_e32 v4, v14
	v_mul_f32_e32 v2, 0xbfb8aa3b, v2
	v_exp_f32_e32 v3, v2
	s_nop 0
	v_cmp_ngt_f32_e32 vcc, s82, v3
	s_and_saveexec_b64 s[4:5], vcc
	s_xor_b64 s[4:5], exec, s[4:5]
	v_add_f32_e32 v2, 1.0, v3
	v_log_f32_e32 v2, v2
	s_nop 0
	v_mul_f32_e32 v2, 0x3f317218, v2
	s_andn2_saveexec_b64 s[4:5], s[4:5]
	v_mov_b32_e32 v2, 0x3e4ccccd
	v_fmamk_f32 v2, v3, 0xbe2aaaab, v2
	v_fma_f32 v2, -v3, v2, s82
	s_mov_b32 s6, 0x3eaaaaab
	v_fma_f32 v2, -v3, v2, s6
	v_fma_f32 v2, -v3, v2, 0.5
	v_fma_f32 v2, -v3, v2, 1.0
	v_mul_f32_e32 v2, v3, v2
	s_or_b64 exec, exec, s[4:5]
	v_mov_b32_e32 v3, v15
	v_mul_f32_e32 v3, 0xbfb8aa3b, v3
	v_exp_f32_e32 v6, v3
	s_nop 0
	v_cmp_ngt_f32_e32 vcc, s82, v6
	s_and_saveexec_b64 s[4:5], vcc
	s_xor_b64 s[4:5], exec, s[4:5]
	v_add_f32_e32 v3, 1.0, v6
	v_log_f32_e32 v3, v3
	s_nop 0
	v_mul_f32_e32 v3, 0x3f317218, v3
	s_andn2_saveexec_b64 s[4:5], s[4:5]
	v_mov_b32_e32 v3, 0x3e4ccccd
	v_fmamk_f32 v3, v6, 0xbe2aaaab, v3
	v_fma_f32 v3, -v6, v3, s82
	s_mov_b32 s6, 0x3eaaaaab
	v_fma_f32 v3, -v6, v3, s6
	v_fma_f32 v3, -v6, v3, 0.5
	v_fma_f32 v3, -v6, v3, 1.0
	v_mul_f32_e32 v3, v6, v3
	s_or_b64 exec, exec, s[4:5]
	s_and_b32 s33, s1, 31
	s_ashr_i32 s28, s1, 9
	v_lshl_or_b32 v16, s33, 7, v144
	s_ashr_i32 s29, s28, 31
	s_lshl_b64 s[4:5], s[28:29], 12
	v_cmp_gt_u32_e32 vcc, 3, v16
	v_or_b32_e32 v6, s4, v16
	v_mov_b32_e32 v7, s5
	v_cndmask_b32_e64 v9, -1, 0, vcc
	v_cndmask_b32_e64 v8, -3, 0, vcc
	v_lshl_add_u64 v[8:9], v[8:9], 0, v[6:7]
	v_mov_b64_e32 v[10:11], s[14:15]
	v_mad_u64_u32 v[12:13], s[6:7], v8, s87, v[10:11]
	v_mad_i32_i24 v13, v9, s87, v13
	s_lshl_b32 s6, s30, 1
	s_mov_b32 s7, s40
	v_cmp_gt_u32_e32 vcc, 2, v16
	v_lshl_add_u64 v[8:9], v[12:13], 0, s[6:7]
	v_mov_b32_e32 v153, v233
	v_cndmask_b32_e64 v13, -1, 0, vcc
	v_cndmask_b32_e64 v12, -2, 0, vcc
	v_lshl_add_u64 v[12:13], v[12:13], 0, v[6:7]
	v_mad_u64_u32 v[14:15], s[10:11], v12, s87, v[10:11]
	v_mad_i32_i24 v15, v13, s87, v15
	v_cmp_ne_u32_e32 vcc, 0, v16
	v_lshl_add_u64 v[12:13], v[14:15], 0, s[6:7]
	s_waitcnt lgkmcnt(0)
	v_lshl_add_u64 v[8:9], v[8:9], 0, v[152:153]
	v_cndmask_b32_e64 v14, 0, 1, vcc
	v_sub_co_u32_e32 v14, vcc, v6, v14
	v_mad_u64_u32 v[14:15], s[10:11], v14, s87, v[10:11]
	s_nop 0
	v_subbrev_co_u32_e32 v7, vcc, 0, v7, vcc
	v_mad_i32_i24 v15, v7, s87, v15
	v_mad_u64_u32 v[6:7], s[10:11], v6, s87, v[10:11]
	v_mov_b32_e32 v10, 0x2c00
	v_mad_i32_i24 v7, s5, v10, v7
	v_lshl_add_u64 v[14:15], v[14:15], 0, s[6:7]
	v_lshl_add_u64 v[6:7], v[6:7], 0, s[6:7]
	v_lshl_add_u64 v[12:13], v[12:13], 0, v[152:153]
	v_lshl_add_u64 v[14:15], v[14:15], 0, v[152:153]
	v_lshl_add_u64 v[6:7], v[6:7], 0, v[152:153]
	global_load_dwordx4 v[60:63], v[8:9], off offset:3072
	global_load_dwordx4 v[64:67], v[8:9], off offset:3104
	global_load_dwordx4 v[68:71], v[12:13], off offset:3072
	global_load_dwordx4 v[72:75], v[12:13], off offset:3104
	global_load_dwordx4 v[76:79], v[14:15], off offset:3072
	global_load_dwordx4 v[80:83], v[14:15], off offset:3104
	global_load_dwordx4 v[84:87], v[6:7], off offset:3072
	global_load_dwordx4 v[88:91], v[6:7], off offset:3104
	global_load_dwordx4 v[92:95], v[8:9], off offset:3136
	global_load_dwordx4 v[96:99], v[8:9], off offset:3168
	global_load_dwordx4 v[100:103], v[12:13], off offset:3136
	global_load_dwordx4 v[104:107], v[12:13], off offset:3168
	global_load_dwordx4 v[108:111], v[14:15], off offset:3136
	global_load_dwordx4 v[112:115], v[14:15], off offset:3168
	global_load_dwordx4 v[116:119], v[6:7], off offset:3136
	global_load_dwordx4 v[120:123], v[6:7], off offset:3168
	s_and_b32 s5, s13, 31
	s_lshl_b32 s6, s5, 7
	v_mul_f32_e32 v203, 0xbfb8aa3b, v0
	v_or_b32_e32 v0, s6, v182
	s_lshr_b32 s4, s1, 5
	v_mul_f32_e32 v153, 0xc138aa3b, v2
	v_lshlrev_b32_e32 v2, 10, v0
	v_or_b32_e32 v0, s6, v196
	s_waitcnt vmcnt(16)
	v_mul_f32_e32 v202, 0xbfb8aa3b, v5
	s_and_b32 s7, s4, 15
	v_lshlrev_b32_e32 v5, 10, v0
	v_or_b32_e32 v0, s6, v194
	v_mul_f32_e32 v192, 0xbfb8aa3b, v4
	v_or_b32_e32 v205, s6, v144
	s_lshl_b32 s4, s7, 7
	v_lshl_or_b32 v4, s7, 6, v183
	v_lshlrev_b32_e32 v6, 10, v0
	v_or_b32_e32 v0, s6, v190
	s_mul_hi_i32 s6, s28, 0x2c00000
	s_mul_i32 s7, s28, 0x2c00000
	v_mul_f32_e32 v204, 0xbfb8aa3b, v1
	v_lshlrev_b32_e32 v7, 10, v0
	v_mov_b32_e32 v1, s6
	v_or_b32_e32 v0, s7, v150
	s_mov_b32 s5, s40
	v_mad_u64_u32 v[0:1], s[6:7], v205, s87, v[0:1]
	v_lshl_add_u64 v[154:155], v[0:1], 0, s[4:5]
	s_lshl_b64 s[4:5], s[28:29], 22
	v_or3_b32 v0, s4, v2, v4
	v_mov_b32_e32 v1, s5
	v_lshlrev_b64 v[156:157], 1, v[0:1]
	v_or3_b32 v0, s4, v5, v4
	v_lshlrev_b64 v[158:159], 1, v[0:1]
	v_or3_b32 v0, s4, v6, v4
	v_lshlrev_b64 v[160:161], 1, v[0:1]
	v_or3_b32 v0, s4, v7, v4
	v_mul_f32_e32 v206, 0xc138aa3b, v3
	s_mov_b32 s34, 0
	v_lshlrev_b64 v[162:163], 1, v[0:1]
	v_mov_b32_e32 v171, 0
	v_mov_b32_e32 v168, 1.0
	v_mov_b32_e32 v164, 1.0
	v_mov_b32_e32 v167, 0
	s_branch .LBB0_605
